# P5 compact path: the 24 per-lane candidate reads from the LDS column issued in two batches of 12 with counted lgkmcnt waits instead of one full wait per read
# baseline (speedup 1.0000x reference)
.LBB0_542:
	s_or_saveexec_b64 s[12:13], s[12:13]
	s_nop 0
	v_mov_b32_e32 v144, s18
	v_mov_b32_e32 v145, s17
	s_xor_b64 exec, exec, s[12:13]
	s_cbranch_execz .LBB0_546
	ds_read_b32 v144, v8 offset:8192
	ds_read_b32 v146, v8 offset:8448
	ds_read_b32 v145, v8 offset:8704
	ds_read_b32 v147, v8 offset:8960
	ds_read_b32 v149, v8 offset:9216
	ds_read_b32 v150, v8 offset:9472
	ds_read_b32 v151, v8 offset:9728
	ds_read_b32 v152, v8 offset:9984
	ds_read_b32 v153, v8 offset:10240
	ds_read_b32 v154, v8 offset:10496
	ds_read_b32 v155, v8 offset:10752
	ds_read_b32 v156, v8 offset:11008
	v_cmp_lt_u32_e32 vcc, s30, v148
	s_waitcnt lgkmcnt(11)
	s_nop 0
	v_cndmask_b32_e32 v144, 0, v144, vcc
	v_cmp_lt_u32_e32 vcc, s36, v148
	s_waitcnt lgkmcnt(10)
	s_nop 0
	v_cndmask_b32_e32 v146, 0, v146, vcc
	v_cmp_lt_u32_e32 vcc, s37, v148
	s_waitcnt lgkmcnt(9)
	s_nop 0
	v_cndmask_b32_e32 v145, 0, v145, vcc
	v_cmp_lt_u32_e32 vcc, s64, v148
	s_waitcnt lgkmcnt(8)
	s_nop 0
	v_cndmask_b32_e32 v147, 0, v147, vcc
	v_cmp_lt_u32_e32 vcc, s38, v148
	s_waitcnt lgkmcnt(7)
	s_nop 0
	v_cndmask_b32_e32 v149, 0, v149, vcc
	v_cmp_lt_u32_e32 vcc, s39, v148
	s_waitcnt lgkmcnt(6)
	s_nop 0
	v_cndmask_b32_e32 v150, 0, v150, vcc
	v_cmp_lt_u32_e32 vcc, s40, v148
	s_waitcnt lgkmcnt(5)
	s_nop 0
	v_cndmask_b32_e32 v151, 0, v151, vcc
	v_cmp_lt_u32_e32 vcc, s31, v148
	s_waitcnt lgkmcnt(4)
	s_nop 0
	v_cndmask_b32_e32 v152, 0, v152, vcc
	v_cmp_lt_u32_e32 vcc, s41, v148
	s_waitcnt lgkmcnt(3)
	s_nop 0
	v_cndmask_b32_e32 v153, 0, v153, vcc
	v_cmp_lt_u32_e32 vcc, s42, v148
	s_waitcnt lgkmcnt(2)
	s_nop 0
	v_cndmask_b32_e32 v154, 0, v154, vcc
	v_cmp_lt_u32_e32 vcc, s43, v148
	s_waitcnt lgkmcnt(1)
	s_nop 0
	v_cndmask_b32_e32 v155, 0, v155, vcc
	v_cmp_lt_u32_e32 vcc, s65, v148
	s_waitcnt lgkmcnt(0)
	s_nop 0
	v_cndmask_b32_e32 v156, 0, v156, vcc
	ds_read_b32 v157, v8 offset:11264
	ds_read_b32 v158, v8 offset:11520
	ds_read_b32 v159, v8 offset:11776
	ds_read_b32 v160, v8 offset:12032
	ds_read_b32 v161, v8 offset:12288
	ds_read_b32 v162, v8 offset:12544
	ds_read_b32 v163, v8 offset:12800
	ds_read_b32 v164, v8 offset:13056
	ds_read_b32 v165, v8 offset:13312
	ds_read_b32 v166, v8 offset:13568
	ds_read_b32 v167, v8 offset:13824
	ds_read_b32 v168, v8 offset:14080
	v_cmp_lt_u32_e32 vcc, s49, v148
	s_waitcnt lgkmcnt(11)
	s_nop 0
	v_cndmask_b32_e32 v157, 0, v157, vcc
	v_cmp_lt_u32_e32 vcc, s53, v148
	s_waitcnt lgkmcnt(10)
	s_nop 0
	v_cndmask_b32_e32 v158, 0, v158, vcc
	v_cmp_lt_u32_e32 vcc, s54, v148
	s_waitcnt lgkmcnt(9)
	s_nop 0
	v_cndmask_b32_e32 v159, 0, v159, vcc
	v_cmp_lt_u32_e32 vcc, s55, v148
	s_waitcnt lgkmcnt(8)
	s_nop 0
	v_cndmask_b32_e32 v160, 0, v160, vcc
	v_cmp_lt_u32_e32 vcc, s56, v148
	s_waitcnt lgkmcnt(7)
	s_nop 0
	v_cndmask_b32_e32 v161, 0, v161, vcc
	v_cmp_lt_u32_e32 vcc, s57, v148
	s_waitcnt lgkmcnt(6)
	s_nop 0
	v_cndmask_b32_e32 v162, 0, v162, vcc
	v_cmp_lt_u32_e32 vcc, s58, v148
	s_waitcnt lgkmcnt(5)
	s_nop 0
	v_cndmask_b32_e32 v163, 0, v163, vcc
	v_cmp_lt_u32_e32 vcc, s67, v148
	s_waitcnt lgkmcnt(4)
	s_nop 0
	v_cndmask_b32_e32 v164, 0, v164, vcc
	v_cmp_lt_u32_e32 vcc, s59, v148
	s_waitcnt lgkmcnt(3)
	s_nop 0
	v_cndmask_b32_e32 v165, 0, v165, vcc
	v_cmp_lt_u32_e32 vcc, s60, v148
	s_waitcnt lgkmcnt(2)
	s_nop 0
	v_cndmask_b32_e32 v166, 0, v166, vcc
	v_cmp_lt_u32_e32 vcc, s61, v148
	s_waitcnt lgkmcnt(1)
	s_nop 0
	v_cndmask_b32_e32 v167, 0, v167, vcc
	v_cmp_lt_u32_e32 vcc, s34, v148
	s_waitcnt lgkmcnt(0)
	s_nop 0
	v_cndmask_b32_e32 v148, 0, v168, vcc
	s_cmp_lt_i32 s16, 0
	s_cbranch_scc1 .LBB0_545
